# speedup vs baseline: 1.0175x; 1.0149x over previous
.LBB0_8:
	s_nop 0
	s_load_dwordx2 s[10:11], s[10:11], 0x0
	s_ashr_i32 s7, s6, 31
	s_lshl_b64 s[6:7], s[6:7], 13
	v_lshl_or_b32 v12, v0, 3, s6
	v_mov_b32_e32 v13, s7
	s_waitcnt lgkmcnt(0)
	v_lshl_add_u64 v[14:15], v[12:13], 2, s[10:11]
	global_load_dwordx4 v[2:5], v[14:15], off offset:16 nt
	global_load_dwordx4 v[6:9], v[14:15], off nt
	s_load_dwordx2 s[6:7], s[4:5], 0x0
	s_cmp_lg_u64 s[8:9], 0
	s_cselect_b64 s[4:5], -1, 0
	s_and_b64 vcc, exec, s[4:5]
	v_lshl_add_u64 v[10:11], v[12:13], 1, s[8:9]
	s_cbranch_vccz .LBB0_10
	s_waitcnt vmcnt(0)
	v_cvt_pk_f16_f32 v16, v6, v7
	v_cvt_pk_f16_f32 v17, v8, v9
	v_cvt_pk_f16_f32 v18, v2, v3
	v_cvt_pk_f16_f32 v19, v4, v5
	global_store_dwordx4 v[10:11], v[16:19], off sc0 sc1
.LBB0_10:
	s_nop 1
	v_mov_b32_e32 v17, 0
	v_mov_b32_e32 v16, 0
	s_waitcnt vmcnt(0)
	v_cvt_pk_fp8_f32 v16, v6, v7
	v_cvt_pk_fp8_f32 v17, v2, v3
	s_waitcnt lgkmcnt(0)
	v_lshl_add_u64 v[12:13], s[6:7], 0, v[12:13]
	v_add_co_u32_e32 v18, vcc, 0x2000, v14
	v_cvt_pk_fp8_f32 v16, v8, v9 op_sel:[0,0,1]
	v_cvt_pk_fp8_f32 v17, v4, v5 op_sel:[0,0,1]
	s_mov_b64 s[6:7], 0x2000
	v_addc_co_u32_e32 v19, vcc, 0, v15, vcc
	global_store_dwordx2 v[12:13], v[16:17], off sc0 sc1
	v_lshl_add_u64 v[16:17], v[14:15], 0, s[6:7]
	global_load_dwordx4 v[2:5], v[18:19], off nt
	global_load_dwordx4 v[6:9], v[16:17], off offset:16 nt
	s_and_b64 vcc, exec, s[4:5]
	s_cbranch_vccz .LBB0_12
	v_add_co_u32_e32 v20, vcc, 0x1000, v10
	s_waitcnt vmcnt(1)
	v_cvt_pk_f16_f32 v16, v2, v3
	v_cvt_pk_f16_f32 v17, v4, v5
	s_waitcnt vmcnt(0)
	v_cvt_pk_f16_f32 v18, v6, v7
	v_cvt_pk_f16_f32 v19, v8, v9
	v_addc_co_u32_e32 v21, vcc, 0, v11, vcc
	global_store_dwordx4 v[20:21], v[16:19], off sc0 sc1
.LBB0_12:
	s_nop 1
	v_mov_b32_e32 v17, 0
	v_mov_b32_e32 v16, 0
	s_waitcnt vmcnt(1)
	v_cvt_pk_fp8_f32 v16, v2, v3
	s_waitcnt vmcnt(0)
	v_cvt_pk_fp8_f32 v17, v6, v7
	s_mov_b64 s[6:7], 0x4000
	v_lshl_add_u64 v[18:19], v[14:15], 0, s[6:7]
	v_cvt_pk_fp8_f32 v16, v4, v5 op_sel:[0,0,1]
	v_cvt_pk_fp8_f32 v17, v8, v9 op_sel:[0,0,1]
	global_store_dwordx2 v[12:13], v[16:17], off offset:2048 sc0 sc1
	v_add_co_u32_e32 v16, vcc, 0x4000, v14
	s_nop 1
	v_addc_co_u32_e32 v17, vcc, 0, v15, vcc
	global_load_dwordx4 v[2:5], v[16:17], off nt
	global_load_dwordx4 v[6:9], v[18:19], off offset:16 nt
	s_and_b64 vcc, exec, s[4:5]
	s_cbranch_vccz .LBB0_14
	v_add_co_u32_e32 v20, vcc, 0x2000, v10
	s_waitcnt vmcnt(1)
	v_cvt_pk_f16_f32 v16, v2, v3
	v_cvt_pk_f16_f32 v17, v4, v5
	s_waitcnt vmcnt(0)
	v_cvt_pk_f16_f32 v18, v6, v7
	v_cvt_pk_f16_f32 v19, v8, v9
	v_addc_co_u32_e32 v21, vcc, 0, v11, vcc
	global_store_dwordx4 v[20:21], v[16:19], off sc0 sc1
.LBB0_14:
	s_nop 1
	v_mov_b32_e32 v17, 0
	v_mov_b32_e32 v16, 0
	s_waitcnt vmcnt(1)
	v_cvt_pk_fp8_f32 v16, v2, v3
	s_waitcnt vmcnt(0)
	v_cvt_pk_fp8_f32 v17, v6, v7
	v_add_co_u32_e32 v2, vcc, 0x1000, v12
	v_cvt_pk_fp8_f32 v16, v4, v5 op_sel:[0,0,1]
	v_cvt_pk_fp8_f32 v17, v8, v9 op_sel:[0,0,1]
	v_addc_co_u32_e32 v3, vcc, 0, v13, vcc
	s_mov_b64 s[6:7], 0x6000
	global_store_dwordx2 v[2:3], v[16:17], off sc0 sc1
	v_lshl_add_u64 v[16:17], v[14:15], 0, s[6:7]
	v_add_co_u32_e32 v14, vcc, 0x6000, v14
	s_nop 1
	v_addc_co_u32_e32 v15, vcc, 0, v15, vcc
	global_load_dwordx4 v[2:5], v[14:15], off nt
	global_load_dwordx4 v[6:9], v[16:17], off offset:16 nt
	s_and_b64 vcc, exec, s[4:5]
	s_cbranch_vccz .LBB0_16
	v_add_co_u32_e32 v10, vcc, 0x3000, v10
	s_waitcnt vmcnt(1)
	v_cvt_pk_f16_f32 v14, v2, v3
	v_cvt_pk_f16_f32 v15, v4, v5
	s_waitcnt vmcnt(0)
	v_cvt_pk_f16_f32 v16, v6, v7
	v_cvt_pk_f16_f32 v17, v8, v9
	v_addc_co_u32_e32 v11, vcc, 0, v11, vcc
	global_store_dwordx4 v[10:11], v[14:17], off sc0 sc1
.LBB0_16:
	v_mov_b32_e32 v11, 0
	v_mov_b32_e32 v10, 0
	s_waitcnt vmcnt(1)
	v_cvt_pk_fp8_f32 v10, v2, v3
	s_waitcnt vmcnt(0)
	v_cvt_pk_fp8_f32 v11, v6, v7
	v_add_co_u32_e32 v2, vcc, 0x1000, v12
	v_cvt_pk_fp8_f32 v10, v4, v5 op_sel:[0,0,1]
	v_cvt_pk_fp8_f32 v11, v8, v9 op_sel:[0,0,1]
	v_addc_co_u32_e32 v3, vcc, 0, v13, vcc
	global_store_dwordx2 v[2:3], v[10:11], off offset:2048 sc0 sc1
	s_branch .LBB0_4

.LBB0_29:
	s_load_dword s1, s[20:21], 0x0
	s_load_dword s0, s[26:27], 0x0
	s_load_dwordx2 s[8:9], s[10:11], 0x0
	v_lshlrev_b32_e32 v2, 2, v0
	v_lshrrev_b32_e32 v22, 2, v0
	s_waitcnt lgkmcnt(0)
	s_ashr_i32 s3, s1, 31
	s_lshr_b32 s3, s3, 26
	s_add_i32 s3, s1, s3
	s_ashr_i32 s3, s3, 6
	s_abs_i32 s12, s3
	v_cvt_f32_u32_e32 v1, s12
	s_sub_i32 s11, 0, s12
	s_sub_i32 s2, s2, s0
	s_abs_i32 s0, s2
	v_rcp_iflag_f32_e32 v1, v1
	s_xor_b32 s10, s2, s3
	s_ashr_i32 s10, s10, 31
	v_and_b32_e32 v20, 60, v2
	v_mul_f32_e32 v1, 0x4f7ffffe, v1
	v_cvt_u32_f32_e32 v1, v1
	v_lshlrev_b32_e32 v18, 2, v20
	v_mov_b32_e32 v19, 0
	v_mov_b32_e32 v23, v19
	v_readfirstlane_b32 s13, v1
	s_mul_i32 s11, s11, s13
	s_mul_hi_u32 s11, s13, s11
	s_add_i32 s13, s13, s11
	s_mul_hi_u32 s11, s0, s13
	s_mul_i32 s13, s11, s12
	s_sub_i32 s0, s0, s13
	s_add_i32 s14, s11, 1
	s_sub_i32 s13, s0, s12
	s_cmp_ge_u32 s0, s12
	s_cselect_b32 s11, s14, s11
	s_cselect_b32 s0, s13, s0
	s_add_i32 s13, s11, 1
	s_cmp_ge_u32 s0, s12
	s_cselect_b32 s0, s13, s11
	s_xor_b32 s0, s0, s10
	s_sub_i32 s0, s0, s10
	s_mul_i32 s3, s0, s3
	s_sub_i32 s2, s2, s3
	s_lshl_b32 s2, s2, 6
	s_ashr_i32 s3, s2, 31
	s_lshl_b32 s0, s0, 6
	s_lshl_b64 s[10:11], s[2:3], 2
	v_and_b32_e32 v1, 60, v22
	s_add_u32 s8, s8, s10
	v_or_b32_e32 v16, s0, v1
	s_addc_u32 s9, s9, s11
	v_lshl_add_u64 v[14:15], s[8:9], 0, v[18:19]
	v_mad_i64_i32 v[2:3], s[8:9], v16, s1, 0
	v_lshl_add_u64 v[10:11], v[2:3], 2, v[14:15]
	v_or_b32_e32 v2, 1, v16
	v_mad_i64_i32 v[2:3], s[8:9], v2, s1, 0
	v_lshl_add_u64 v[12:13], v[2:3], 2, v[14:15]
	global_load_dwordx4 v[2:5], v[10:11], off nt
	global_load_dwordx4 v[6:9], v[12:13], off nt
	v_or_b32_e32 v10, 2, v16
	v_or_b32_e32 v16, 3, v16
	v_mad_i64_i32 v[10:11], s[8:9], v10, s1, 0
	v_mad_i64_i32 v[16:17], s[8:9], v16, s1, 0
	v_lshl_add_u64 v[10:11], v[10:11], 2, v[14:15]
	v_lshl_add_u64 v[14:15], v[16:17], 2, v[14:15]
	global_load_dwordx4 v[10:13], v[10:11], off nt
	v_lshlrev_b32_e32 v18, 4, v0
	global_load_dwordx4 v[14:17], v[14:15], off nt
	s_load_dword s1, s[6:7], 0x0
	s_load_dwordx2 s[8:9], s[4:5], 0x0
	s_mov_b32 s4, 0x42000000
	v_mov_b32_e32 v24, v19
	v_mul_u32_u24_e32 v0, 0x50, v20
	v_mov_b32_e32 v25, v19
	v_mov_b32_e32 v26, v19
	v_or_b32_e32 v27, v0, v1
	s_movk_i32 s3, 0x50
	v_and_b32_e32 v18, 48, v18
	s_waitcnt lgkmcnt(0)
	v_mov_b64_e32 v[20:21], s[8:9]
	v_or_b32_e32 v28, s2, v22
	s_waitcnt vmcnt(3)
	v_pk_mul_f32 v[2:3], v[2:3], s[4:5] op_sel_hi:[1,0]
	s_waitcnt vmcnt(2)
	v_pk_mul_f32 v[6:7], v[6:7], s[4:5] op_sel_hi:[1,0]
	v_pk_mul_f32 v[0:1], v[4:5], s[4:5] op_sel_hi:[1,0]
	v_pk_mul_f32 v[4:5], v[8:9], s[4:5] op_sel_hi:[1,0]
	v_cvt_pk_fp8_f32 v23, v2, v6
	v_cvt_pk_fp8_f32 v24, v3, v7
	v_cvt_pk_fp8_f32 v25, v0, v4
	v_cvt_pk_fp8_f32 v26, v1, v5
	v_mad_u32_u24 v0, v22, s3, v18
	v_mad_i64_i32 v[4:5], s[2:3], v28, s1, v[20:21]
	s_waitcnt vmcnt(1)
	v_pk_mul_f32 v[10:11], v[10:11], s[4:5] op_sel_hi:[1,0]
	s_waitcnt vmcnt(0)
	v_pk_mul_f32 v[14:15], v[14:15], s[4:5] op_sel_hi:[1,0]
	v_pk_mul_f32 v[8:9], v[12:13], s[4:5] op_sel_hi:[1,0]
	v_pk_mul_f32 v[12:13], v[16:17], s[4:5] op_sel_hi:[1,0]
	v_cvt_pk_fp8_f32 v23, v10, v14 op_sel:[0,0,1]
	v_cvt_pk_fp8_f32 v24, v11, v15 op_sel:[0,0,1]
	v_cvt_pk_fp8_f32 v25, v8, v12 op_sel:[0,0,1]
	v_cvt_pk_fp8_f32 v26, v9, v13 op_sel:[0,0,1]
	ds_write2_b32 v27, v23, v24 offset1:20
	ds_write2_b32 v27, v25, v26 offset0:40 offset1:60
	s_waitcnt lgkmcnt(0)
	s_barrier
	ds_read_b128 v[0:3], v0
	s_ashr_i32 s1, s0, 31
	v_lshl_add_u64 v[4:5], v[4:5], 0, s[0:1]
	v_lshl_add_u64 v[4:5], v[4:5], 0, v[18:19]
	s_waitcnt lgkmcnt(0)
	global_store_dwordx4 v[4:5], v[0:3], off sc0 sc1
	s_endpgm

.LBB0_35:
	s_add_u32 s10, s0, 0x100
	s_addc_u32 s11, s1, 0
	s_add_u32 s4, s0, 0x108
	s_addc_u32 s5, s1, 0
	s_add_u32 s6, s0, 0x110
	s_addc_u32 s7, s1, 0
	s_add_u32 s20, s0, 0x114
	s_addc_u32 s21, s1, 0
	s_mov_b64 s[26:27], s[12:13]
	s_cmp_lg_u32 s3, 9
	s_cbranch_scc0 .LBB0_28
	s_branch .LBB0_29
	.p2align	8

.LBB1_3:
	s_load_dwordx2 s[10:11], s[0:1], 0x28
	s_cmp_lg_u64 s[4:5], 0
	s_cselect_b64 s[0:1], -1, 0
	s_cmp_eq_u64 s[4:5], 0
	v_lshl_add_u64 v[22:23], v[30:31], 1, s[4:5]
	v_lshlrev_b32_e32 v24, 1, v8
	s_cbranch_scc1 .LBB1_5
	v_mov_b32_e32 v25, 0
	v_cvt_pk_f16_f32 v32, v4, v5
	v_cvt_pk_f16_f32 v33, v6, v7
	v_cvt_pk_f16_f32 v34, v0, v1
	v_cvt_pk_f16_f32 v35, v2, v3
	v_lshl_add_u64 v[36:37], v[22:23], 0, v[24:25]
	global_store_dwordx4 v[36:37], v[32:35], off sc0 sc1
.LBB1_5:
	s_waitcnt lgkmcnt(0)
	s_cmp_lg_u64 s[10:11], 0
	v_lshl_add_u64 v[30:31], s[10:11], 0, v[30:31]
	v_lshl_add_u64 v[32:33], s[6:7], 0, v[10:11]
	v_lshl_add_u64 v[10:11], s[8:9], 0, v[10:11]
	v_mov_b32_e32 v29, v28
	s_cselect_b64 s[4:5], -1, 0
	s_cmp_eq_u64 s[10:11], 0
	v_lshl_add_u64 v[8:9], v[30:31], 0, v[8:9]
	s_cbranch_scc1 .LBB1_7
	v_mov_b32_e32 v31, 0
	v_mov_b32_e32 v30, 0
	v_cvt_pk_fp8_f32 v30, v4, v5
	v_cvt_pk_fp8_f32 v31, v0, v1
	v_cvt_pk_fp8_f32 v30, v6, v7 op_sel:[0,0,1]
	v_cvt_pk_fp8_f32 v31, v2, v3 op_sel:[0,0,1]
	global_store_dwordx2 v[8:9], v[30:31], off sc0 sc1

.LBB1_9:
	s_andn2_b64 vcc, exec, s[0:1]
	s_cbranch_vccnz .LBB1_11
	v_mov_b32_e32 v25, 0
	v_cvt_pk_f16_f32 v10, v4, v5
	v_cvt_pk_f16_f32 v11, v6, v7
	v_cvt_pk_f16_f32 v12, v0, v1
	v_cvt_pk_f16_f32 v13, v2, v3
	v_lshl_add_u64 v[14:15], v[22:23], 0, v[24:25]
	global_store_dwordx4 v[14:15], v[10:13], off offset:1024 sc0 sc1
.LBB1_11:
	s_andn2_b64 vcc, exec, s[4:5]
	s_cbranch_vccnz .LBB1_13
	v_mov_b32_e32 v11, 0
	v_mov_b32_e32 v10, 0
	v_cvt_pk_fp8_f32 v10, v4, v5
	v_cvt_pk_fp8_f32 v11, v0, v1
	v_cvt_pk_fp8_f32 v10, v6, v7 op_sel:[0,0,1]
	v_cvt_pk_fp8_f32 v11, v2, v3 op_sel:[0,0,1]
	global_store_dwordx2 v[8:9], v[10:11], off offset:512 sc0 sc1

.LBB3_36:
	v_add_f32_e32 v64, v48, v49
	v_add_f32_e32 v64, v50, v64
	v_add_f32_e32 v64, v51, v64
	v_add_f32_e32 v64, v52, v64
	v_add_f32_e32 v68, v53, v64
	v_cvt_pk_f16_f32 v48, v48, v49
	v_cvt_pk_f16_f32 v49, v50, v51
	v_cvt_pk_f16_f32 v50, v52, v53
	v_cvt_pk_f16_f32 v51, v54, v55
	ds_read_b64_tr_b16 v[64:65], v207 offset:24576
	ds_read_b64_tr_b16 v[66:67], v207 offset:25088
	v_add_f32_e32 v52, v54, v68
	v_add_f32_e32 v68, v55, v52
	ds_read_b64_tr_b16 v[52:53], v207 offset:25600
	ds_read_b64_tr_b16 v[54:55], v207 offset:26112
	s_waitcnt lgkmcnt(2)
	v_mfma_f32_32x32x16_f16 v[0:15], v[48:51], v[64:67], v[0:15]
	ds_read_b64_tr_b16 v[64:65], v207 offset:28672
	ds_read_b64_tr_b16 v[66:67], v207 offset:29184
	v_add_f32_e32 v68, v56, v68
	v_add_f32_e32 v73, v57, v68
	v_cvt_pk_f16_f32 v68, v56, v57
	v_cvt_pk_f16_f32 v69, v58, v59
	v_cvt_pk_f16_f32 v70, v60, v61
	v_cvt_pk_f16_f32 v71, v62, v63
	s_waitcnt lgkmcnt(0)
	v_mfma_f32_32x32x16_f16 v[16:31], v[48:51], v[64:67], v[16:31]
	v_add_f32_e32 v48, v58, v73
	v_add_f32_e32 v48, v59, v48
	v_add_f32_e32 v48, v60, v48
	v_add_f32_e32 v48, v61, v48
	ds_read_b64_tr_b16 v[74:75], v207 offset:29696
	ds_read_b64_tr_b16 v[76:77], v207 offset:30208
	v_add_f32_e32 v48, v62, v48
	v_add_f32_e32 v48, v63, v48
	v_mfma_f32_32x32x16_f16 v[0:15], v[68:71], v[52:55], v[0:15]
	v_add_f32_e32 v48, v32, v48
	v_add_f32_e32 v56, v33, v48
	v_cvt_pk_f16_f32 v48, v32, v33
	v_cvt_pk_f16_f32 v49, v34, v35
	v_cvt_pk_f16_f32 v50, v36, v37
	v_cvt_pk_f16_f32 v51, v38, v39
	ds_read_b64_tr_b16 v[52:53], v207 offset:26624
	ds_read_b64_tr_b16 v[54:55], v207 offset:27136
	s_waitcnt lgkmcnt(2)
	v_mfma_f32_32x32x16_f16 v[16:31], v[68:71], v[74:77], v[16:31]
	v_add_f32_e32 v32, v34, v56
	v_add_f32_e32 v56, v35, v32
	ds_read_b64_tr_b16 v[32:33], v207 offset:27648
	ds_read_b64_tr_b16 v[34:35], v207 offset:28160
	v_add_f32_e32 v36, v36, v56
	v_add_f32_e32 v36, v37, v36
	v_cvt_pk_f16_f32 v56, v40, v41
	v_cvt_pk_f16_f32 v57, v42, v43
	s_waitcnt lgkmcnt(2)
	v_mfma_f32_32x32x16_f16 v[0:15], v[48:51], v[52:55], v[0:15]
	ds_read_b64_tr_b16 v[52:53], v207 offset:30720
	ds_read_b64_tr_b16 v[54:55], v207 offset:31232
	v_cvt_pk_f16_f32 v58, v44, v45
	v_cvt_pk_f16_f32 v59, v46, v47
	ds_read_b64_tr_b16 v[60:61], v207 offset:31744
	ds_read_b64_tr_b16 v[62:63], v207 offset:32256
	v_add_f32_e32 v36, v38, v36
	v_add_f32_e32 v36, v39, v36
	v_add_f32_e32 v36, v40, v36
	s_waitcnt lgkmcnt(2)
	v_mfma_f32_32x32x16_f16 v[16:31], v[48:51], v[52:55], v[16:31]
	v_add_f32_e32 v36, v41, v36
	v_mfma_f32_32x32x16_f16 v[0:15], v[56:59], v[32:35], v[0:15]
	v_add_f32_e32 v32, v42, v36
	v_add_f32_e32 v32, v43, v32
	v_add_f32_e32 v32, v44, v32
	v_add_f32_e32 v32, v45, v32
	v_add_f32_e32 v32, v46, v32
	v_add_f32_e32 v32, v47, v32
	v_add_f32_e32 v32, v72, v32
	s_waitcnt lgkmcnt(0)
	v_mfma_f32_32x32x16_f16 v[16:31], v[56:59], v[60:63], v[16:31]
	v_mov_b32_e32 v33, v32
	s_nop 1
	v_permlane32_swap_b32_e32 v32, v33
	s_and_saveexec_b64 s[2:3], s[0:1]
	v_add_f32_e32 v32, v32, v33
	ds_write_b32 v206, v32 offset:49280
	s_or_b64 exec, exec, s[2:3]
	s_waitcnt lgkmcnt(0)
	ds_read_b128 v[32:35], v205 offset:49280
	ds_read_b128 v[36:39], v205 offset:49312
	s_lshl_b64 s[0:1], s[18:19], 10
	s_add_u32 s0, s16, s0
	s_addc_u32 s1, s17, s1
	s_waitcnt lgkmcnt(1)
	v_rcp_f32_e32 v40, v32
	v_rcp_f32_e32 v41, v33
	v_rcp_f32_e32 v42, v34
	s_lshl_b32 s2, s33, 11
	v_mul_f32_e32 v40, 0x41800000, v40
	v_mul_f32_e32 v0, v0, v40
	v_mul_f32_e32 v16, v16, v40
	v_mov_b32_e32 v40, 0
	v_cvt_pk_fp8_f32 v40, v0, v16
	v_mul_f32_e32 v16, 0x41800000, v41
	v_mul_f32_e32 v1, v1, v16
	v_mul_f32_e32 v16, v17, v16
	v_mov_b32_e32 v17, 0
	v_cvt_pk_fp8_f32 v17, v1, v16
	s_add_i32 s2, s2, 0
	v_lshlrev_b32_e32 v0, 8, v204
	v_rcp_f32_e32 v43, v35
	v_add3_u32 v0, s2, v203, v0
	v_lshrrev_b32_e32 v1, 8, v40
	s_waitcnt lgkmcnt(0)
	v_rcp_f32_e32 v44, v36
	ds_read_b128 v[32:35], v205 offset:49344
	v_rcp_f32_e32 v45, v37
	v_rcp_f32_e32 v46, v38
	v_rcp_f32_e32 v47, v39
	ds_read_b128 v[36:39], v205 offset:49376
	s_waitcnt lgkmcnt(0)
	s_barrier
	ds_write_b8 v0, v40 offset:51200
	ds_write_b8 v0, v1 offset:51232
	ds_write_b8 v0, v17 offset:51264
	v_lshrrev_b32_e32 v1, 8, v17
	ds_write_b8 v0, v1 offset:51296
	v_mul_f32_e32 v1, 0x41800000, v42
	v_mul_f32_e32 v2, v2, v1
	v_mul_f32_e32 v1, v18, v1
	v_mov_b32_e32 v16, 0
	v_cvt_pk_fp8_f32 v16, v2, v1
	v_mul_f32_e32 v1, 0x41800000, v43
	v_mul_f32_e32 v2, v3, v1
	v_mul_f32_e32 v1, v19, v1
	v_mov_b32_e32 v3, 0
	v_cvt_pk_fp8_f32 v3, v2, v1
	v_lshrrev_b32_e32 v1, 8, v16
	ds_write_b8 v0, v16 offset:51328
	ds_write_b8 v0, v1 offset:51360
	ds_write_b8 v0, v3 offset:51392
	v_lshrrev_b32_e32 v1, 8, v3
	ds_write_b8 v0, v1 offset:51424
	v_mul_f32_e32 v1, 0x41800000, v44
	v_mul_f32_e32 v2, v4, v1
	v_mul_f32_e32 v1, v20, v1
	v_mov_b32_e32 v3, 0
	v_cvt_pk_fp8_f32 v3, v2, v1
	v_mul_f32_e32 v1, 0x41800000, v45
	v_mul_f32_e32 v2, v5, v1
	v_mul_f32_e32 v1, v21, v1
	v_mov_b32_e32 v4, 0
	v_cvt_pk_fp8_f32 v4, v2, v1
	v_lshrrev_b32_e32 v1, 8, v3
	ds_write_b8 v0, v3 offset:51712
	ds_write_b8 v0, v1 offset:51744
	ds_write_b8 v0, v4 offset:51776
	v_lshrrev_b32_e32 v1, 8, v4
	ds_write_b8 v0, v1 offset:51808
	v_mul_f32_e32 v1, 0x41800000, v46
	v_mul_f32_e32 v2, v6, v1
	v_mul_f32_e32 v1, v22, v1
	v_mov_b32_e32 v3, 0
	v_cvt_pk_fp8_f32 v3, v2, v1
	v_mul_f32_e32 v1, 0x41800000, v47
	v_mul_f32_e32 v2, v7, v1
	v_mul_f32_e32 v1, v23, v1
	v_mov_b32_e32 v4, 0
	v_cvt_pk_fp8_f32 v4, v2, v1
	s_waitcnt lgkmcnt(13)
	v_rcp_f32_e32 v32, v32
	v_rcp_f32_e32 v33, v33
	v_lshrrev_b32_e32 v1, 8, v3
	ds_write_b8 v0, v3 offset:51840
	ds_write_b8 v0, v1 offset:51872
	ds_write_b8 v0, v4 offset:51904
	v_lshrrev_b32_e32 v1, 8, v4
	ds_write_b8 v0, v1 offset:51936
	v_mul_f32_e32 v1, 0x41800000, v32
	v_mul_f32_e32 v2, v8, v1
	v_mul_f32_e32 v1, v24, v1
	v_mov_b32_e32 v3, 0
	v_cvt_pk_fp8_f32 v3, v2, v1
	v_mul_f32_e32 v1, 0x41800000, v33
	v_mul_f32_e32 v2, v9, v1
	v_mul_f32_e32 v1, v25, v1
	v_mov_b32_e32 v4, 0
	v_cvt_pk_fp8_f32 v4, v2, v1
	v_rcp_f32_e32 v34, v34
	v_rcp_f32_e32 v35, v35
	v_lshrrev_b32_e32 v1, 8, v3
	ds_write_b8 v0, v3 offset:52224
	ds_write_b8 v0, v1 offset:52256
	ds_write_b8 v0, v4 offset:52288
	v_lshrrev_b32_e32 v1, 8, v4
	ds_write_b8 v0, v1 offset:52320
	v_mul_f32_e32 v1, 0x41800000, v34
	v_mul_f32_e32 v2, v10, v1
	v_mul_f32_e32 v1, v26, v1
	v_mov_b32_e32 v3, 0
	v_cvt_pk_fp8_f32 v3, v2, v1
	v_mul_f32_e32 v1, 0x41800000, v35
	v_mul_f32_e32 v2, v11, v1
	v_mul_f32_e32 v1, v27, v1
	v_mov_b32_e32 v4, 0
	v_cvt_pk_fp8_f32 v4, v2, v1
	s_waitcnt lgkmcnt(14)
	v_rcp_f32_e32 v36, v36
	v_rcp_f32_e32 v37, v37
	v_lshrrev_b32_e32 v1, 8, v3
	ds_write_b8 v0, v3 offset:52352
	ds_write_b8 v0, v1 offset:52384
	ds_write_b8 v0, v4 offset:52416
	v_lshrrev_b32_e32 v1, 8, v4
	ds_write_b8 v0, v1 offset:52448
	v_mul_f32_e32 v1, 0x41800000, v36
	v_mul_f32_e32 v2, v12, v1
	v_mul_f32_e32 v1, v28, v1
	v_mov_b32_e32 v3, 0
	v_cvt_pk_fp8_f32 v3, v2, v1
	v_mul_f32_e32 v1, 0x41800000, v37
	v_mul_f32_e32 v2, v13, v1
	v_mul_f32_e32 v1, v29, v1
	v_mov_b32_e32 v4, 0
	v_cvt_pk_fp8_f32 v4, v2, v1
	v_rcp_f32_e32 v38, v38
	v_rcp_f32_e32 v39, v39
	v_lshrrev_b32_e32 v1, 8, v3
	ds_write_b8 v0, v3 offset:52736
	ds_write_b8 v0, v1 offset:52768
	ds_write_b8 v0, v4 offset:52800
	v_lshrrev_b32_e32 v1, 8, v4
	ds_write_b8 v0, v1 offset:52832
	v_mul_f32_e32 v1, 0x41800000, v38
	v_mul_f32_e32 v2, v14, v1
	v_mul_f32_e32 v1, v30, v1
	v_mov_b32_e32 v3, 0
	v_cvt_pk_fp8_f32 v3, v2, v1
	v_mul_f32_e32 v1, 0x41800000, v39
	v_mul_f32_e32 v2, v15, v1
	v_mul_f32_e32 v1, v31, v1
	v_mov_b32_e32 v4, 0
	v_cvt_pk_fp8_f32 v4, v2, v1
	v_lshrrev_b32_e32 v1, 8, v3
	ds_write_b8 v0, v3 offset:52864
	ds_write_b8 v0, v1 offset:52896
	ds_write_b8 v0, v4 offset:52928
	v_lshrrev_b32_e32 v1, 8, v4
	ds_write_b8 v0, v1 offset:52960
	v_add_u32_e32 v4, s2, v160
	s_waitcnt lgkmcnt(0)
	v_lshl_add_u32 v0, v202, 6, v4
	v_or_b32_e32 v12, 16, v202
	ds_read_b128 v[0:3], v0 offset:51200
	v_lshl_add_u32 v4, v12, 6, v4
	s_add_u32 s0, s0, s6
	ds_read_b128 v[4:7], v4 offset:51200
	v_mov_b32_e32 v161, 0
	s_addc_u32 s1, s1, 0
	v_lshl_add_u64 v[8:9], s[0:1], 0, v[160:161]
	v_lshlrev_b32_e32 v160, 10, v202
	v_lshl_add_u64 v[10:11], v[8:9], 0, v[160:161]
	v_lshlrev_b32_e32 v160, 10, v12
	s_waitcnt lgkmcnt(1)
	global_store_dwordx4 v[10:11], v[0:3], off sc0 sc1
	s_nop 1
	v_lshl_add_u64 v[0:1], v[8:9], 0, v[160:161]
	s_waitcnt lgkmcnt(0)
	global_store_dwordx4 v[0:1], v[4:7], off sc0 sc1
	s_waitcnt lgkmcnt(0)
	s_barrier
	s_endpgm

.LBB4_10:
	s_waitcnt vmcnt(0)
	v_cvt_f32_f16_sdwa v45, v34 dst_sel:DWORD dst_unused:UNUSED_PAD src0_sel:WORD_1
	v_cvt_f32_f16_e32 v44, v34
	v_cvt_f32_f16_sdwa v47, v35 dst_sel:DWORD dst_unused:UNUSED_PAD src0_sel:WORD_1
	v_cvt_f32_f16_e32 v46, v35
	v_cvt_f32_f16_sdwa v35, v36 dst_sel:DWORD dst_unused:UNUSED_PAD src0_sel:WORD_1
	v_cvt_f32_f16_e32 v34, v36
	v_pk_add_f32 v[30:31], v[30:31], v[44:45]
	v_cvt_f32_f16_sdwa v45, v37 dst_sel:DWORD dst_unused:UNUSED_PAD src0_sel:WORD_1
	v_cvt_f32_f16_e32 v44, v37
	v_pk_add_f32 v[32:33], v[32:33], v[46:47]
	v_pk_add_f32 v[26:27], v[26:27], v[34:35]
	v_cvt_pk_f16_f32 v30, v30, v31
	v_cvt_pk_f16_f32 v31, v32, v33
	v_cvt_pk_f16_f32 v32, v26, v27
	v_pk_add_f32 v[26:27], v[28:29], v[44:45]
	s_mov_b32 s6, s3
	v_cvt_pk_f16_f32 v33, v26, v27
	v_lshl_add_u64 v[26:27], v[40:41], 1, s[4:5]
	global_store_dwordx4 v[26:27], v[30:33], off sc0 sc1
	v_or_b32_e32 v26, 16, v42
	s_mov_b32 s7, s3
	v_mad_i64_i32 v[30:31], s[0:1], v26, s2, v[38:39]
	v_lshl_add_u64 v[26:27], v[30:31], 1, s[8:9]
	global_load_dwordx4 v[26:29], v[26:27], off
	v_cndmask_b32_e64 v32, 0, 1, s[12:13]
	v_pk_mul_f32 v[24:25], s[6:7], v[24:25]
	v_pk_mul_f32 v[22:23], s[10:11], v[22:23]
	v_pk_mul_f32 v[20:21], s[6:7], v[20:21]
	v_cmp_ne_u32_e64 s[0:1], 1, v32
	s_andn2_b64 vcc, exec, s[12:13]
	v_pk_mul_f32 v[18:19], s[10:11], v[18:19]
	s_cbranch_vccnz .LBB4_12
	global_load_dwordx4 v[32:35], v[0:1], off
	global_load_dwordx4 v[44:47], v[0:1], off offset:16
	s_waitcnt vmcnt(1)
	v_pk_add_f32 v[24:25], v[24:25], v[34:35]
	v_pk_add_f32 v[22:23], v[22:23], v[32:33]
	s_waitcnt vmcnt(0)
	v_pk_add_f32 v[20:21], v[20:21], v[46:47]
	v_pk_add_f32 v[18:19], v[18:19], v[44:45]
.LBB4_12:
	s_waitcnt vmcnt(0)
	v_cvt_f32_f16_sdwa v33, v26 dst_sel:DWORD dst_unused:UNUSED_PAD src0_sel:WORD_1
	v_cvt_f32_f16_e32 v32, v26
	v_cvt_f32_f16_sdwa v35, v27 dst_sel:DWORD dst_unused:UNUSED_PAD src0_sel:WORD_1
	v_cvt_f32_f16_e32 v34, v27
	v_cvt_f32_f16_sdwa v27, v28 dst_sel:DWORD dst_unused:UNUSED_PAD src0_sel:WORD_1
	v_cvt_f32_f16_e32 v26, v28
	v_pk_add_f32 v[22:23], v[22:23], v[32:33]
	v_cvt_f32_f16_sdwa v33, v29 dst_sel:DWORD dst_unused:UNUSED_PAD src0_sel:WORD_1
	v_cvt_f32_f16_e32 v32, v29
	v_pk_add_f32 v[24:25], v[24:25], v[34:35]
	v_pk_add_f32 v[18:19], v[18:19], v[26:27]
	v_cvt_pk_f16_f32 v22, v22, v23
	v_cvt_pk_f16_f32 v23, v24, v25
	v_cvt_pk_f16_f32 v24, v18, v19
	v_pk_add_f32 v[18:19], v[20:21], v[32:33]
	v_pk_mul_f32 v[16:17], s[6:7], v[16:17]
	v_cvt_pk_f16_f32 v25, v18, v19
	v_lshl_add_u64 v[18:19], v[30:31], 1, s[4:5]
	global_store_dwordx4 v[18:19], v[22:25], off sc0 sc1
	v_or_b32_e32 v18, 32, v42
	v_pk_mul_f32 v[14:15], s[10:11], v[14:15]
	v_mad_i64_i32 v[22:23], s[12:13], v18, s2, v[38:39]
	v_lshl_add_u64 v[18:19], v[22:23], 1, s[8:9]
	global_load_dwordx4 v[18:21], v[18:19], off
	v_pk_mul_f32 v[12:13], s[6:7], v[12:13]
	s_and_b64 vcc, exec, s[0:1]
	v_pk_mul_f32 v[10:11], s[10:11], v[10:11]
	s_cbranch_vccnz .LBB4_14
	global_load_dwordx4 v[24:27], v[0:1], off
	global_load_dwordx4 v[28:31], v[0:1], off offset:16
	s_waitcnt vmcnt(1)
	v_pk_add_f32 v[16:17], v[16:17], v[26:27]
	v_pk_add_f32 v[14:15], v[14:15], v[24:25]
	s_waitcnt vmcnt(0)
	v_pk_add_f32 v[12:13], v[12:13], v[30:31]
	v_pk_add_f32 v[10:11], v[10:11], v[28:29]
.LBB4_14:
	s_waitcnt vmcnt(0)
	v_cvt_f32_f16_sdwa v25, v18 dst_sel:DWORD dst_unused:UNUSED_PAD src0_sel:WORD_1
	v_cvt_f32_f16_e32 v24, v18
	v_cvt_f32_f16_sdwa v27, v19 dst_sel:DWORD dst_unused:UNUSED_PAD src0_sel:WORD_1
	v_cvt_f32_f16_e32 v26, v19
	v_cvt_f32_f16_sdwa v19, v20 dst_sel:DWORD dst_unused:UNUSED_PAD src0_sel:WORD_1
	v_cvt_f32_f16_e32 v18, v20
	v_pk_add_f32 v[14:15], v[14:15], v[24:25]
	v_cvt_f32_f16_sdwa v25, v21 dst_sel:DWORD dst_unused:UNUSED_PAD src0_sel:WORD_1
	v_cvt_f32_f16_e32 v24, v21
	v_pk_add_f32 v[16:17], v[16:17], v[26:27]
	v_pk_add_f32 v[10:11], v[10:11], v[18:19]
	v_cvt_pk_f16_f32 v14, v14, v15
	v_cvt_pk_f16_f32 v15, v16, v17
	v_cvt_pk_f16_f32 v16, v10, v11
	v_pk_add_f32 v[10:11], v[12:13], v[24:25]
	v_pk_mul_f32 v[6:7], s[10:11], v[6:7]
	v_cvt_pk_f16_f32 v17, v10, v11
	v_lshl_add_u64 v[10:11], v[22:23], 1, s[4:5]
	global_store_dwordx4 v[10:11], v[14:17], off sc0 sc1
	v_or_b32_e32 v10, 48, v42
	s_and_b64 vcc, exec, s[0:1]
	v_mad_i64_i32 v[14:15], s[6:7], v10, s2, v[38:39]
	v_lshl_add_u64 v[10:11], v[14:15], 1, s[8:9]
	global_load_dwordx4 v[10:13], v[10:11], off
	s_mov_b32 s2, s3
	v_pk_mul_f32 v[8:9], s[2:3], v[8:9]
	v_pk_mul_f32 v[4:5], s[2:3], v[4:5]
	v_pk_mul_f32 v[2:3], s[10:11], v[2:3]
	s_cbranch_vccnz .LBB4_16
	global_load_dwordx4 v[16:19], v[0:1], off
	global_load_dwordx4 v[20:23], v[0:1], off offset:16
	s_waitcnt vmcnt(1)
	v_pk_add_f32 v[8:9], v[8:9], v[18:19]
	v_pk_add_f32 v[6:7], v[6:7], v[16:17]
	s_waitcnt vmcnt(0)
	v_pk_add_f32 v[4:5], v[4:5], v[22:23]
	v_pk_add_f32 v[2:3], v[2:3], v[20:21]
.LBB4_16:
	s_waitcnt vmcnt(0)
	v_cvt_f32_f16_sdwa v1, v10 dst_sel:DWORD dst_unused:UNUSED_PAD src0_sel:WORD_1
	v_cvt_f32_f16_e32 v0, v10
	v_cvt_f32_f16_sdwa v17, v11 dst_sel:DWORD dst_unused:UNUSED_PAD src0_sel:WORD_1
	v_cvt_f32_f16_e32 v16, v11
	v_cvt_f32_f16_sdwa v11, v13 dst_sel:DWORD dst_unused:UNUSED_PAD src0_sel:WORD_1
	v_pk_add_f32 v[0:1], v[6:7], v[0:1]
	v_cvt_f32_f16_e32 v10, v13
	v_pk_add_f32 v[6:7], v[8:9], v[16:17]
	v_cvt_f32_f16_sdwa v9, v12 dst_sel:DWORD dst_unused:UNUSED_PAD src0_sel:WORD_1
	v_cvt_f32_f16_e32 v8, v12
	v_pk_add_f32 v[4:5], v[4:5], v[10:11]
	v_cvt_pk_f16_f32 v0, v0, v1
	v_cvt_pk_f16_f32 v1, v6, v7
	v_pk_add_f32 v[2:3], v[2:3], v[8:9]
	s_nop 0
	v_cvt_pk_f16_f32 v2, v2, v3
	v_cvt_pk_f16_f32 v3, v4, v5
	v_lshl_add_u64 v[4:5], v[14:15], 1, s[4:5]
	global_store_dwordx4 v[4:5], v[0:3], off sc0 sc1
	s_endpgm
	.p2align	8

.LBB5_8:
	v_mov_b32_e32 v33, v35
	s_barrier
	s_nop 15
	s_nop 15
	s_nop 15
	v_lshlrev_b32_e32 v0, 3, v1
	v_mov_b32_e32 v1, 0
	s_waitcnt lgkmcnt(0)
	v_pk_mul_f32 v[30:31], s[2:3], v[30:31] op_sel:[1,0]
	v_pk_mul_f32 v[26:27], s[2:3], v[26:27] op_sel:[1,0]
	v_mov_b32_e32 v34, v1
	v_mov_b32_e32 v35, v1
	v_cvt_pk_fp8_f32 v34, v30, v31
	v_cvt_pk_fp8_f32 v35, v26, v27
	v_pk_mul_f32 v[26:27], s[2:3], v[32:33] op_sel:[1,0]
	v_pk_mul_f32 v[28:29], s[2:3], v[28:29] op_sel:[1,0]
	s_lshl_b32 s4, s9, 7
	v_lshl_or_b32 v0, s8, 7, v0
	v_cvt_pk_fp8_f32 v34, v26, v27 op_sel:[0,0,1]
	v_cvt_pk_fp8_f32 v35, v28, v29 op_sel:[0,0,1]
	s_add_i32 s4, s4, s14
	v_or_b32_e32 v0, s13, v0
	v_or_b32_e32 v36, s4, v42
	v_lshl_add_u64 v[26:27], s[0:1], 0, v[0:1]
	v_mad_i64_i32 v[28:29], s[0:1], v36, s2, v[26:27]
	global_store_dwordx2 v[28:29], v[34:35], off sc0 sc1
	v_pk_mul_f32 v[22:23], s[2:3], v[22:23] op_sel:[1,0]
	v_pk_mul_f32 v[18:19], s[2:3], v[18:19] op_sel:[1,0]
	v_mov_b32_e32 v28, v1
	v_mov_b32_e32 v29, v1
	v_cvt_pk_fp8_f32 v28, v22, v23
	v_cvt_pk_fp8_f32 v29, v18, v19
	v_pk_mul_f32 v[18:19], s[2:3], v[24:25] op_sel:[1,0]
	v_pk_mul_f32 v[20:21], s[2:3], v[20:21] op_sel:[1,0]
	v_cvt_pk_fp8_f32 v28, v18, v19 op_sel:[0,0,1]
	v_cvt_pk_fp8_f32 v29, v20, v21 op_sel:[0,0,1]
	v_or_b32_e32 v0, 16, v36
	v_mad_i64_i32 v[18:19], s[0:1], v0, s2, v[26:27]
	global_store_dwordx2 v[18:19], v[28:29], off sc0 sc1
	v_pk_mul_f32 v[14:15], s[2:3], v[14:15] op_sel:[1,0]
	v_mov_b32_e32 v18, v1
	v_cvt_pk_fp8_f32 v18, v14, v15
	v_pk_mul_f32 v[10:11], s[2:3], v[10:11] op_sel:[1,0]
	v_mov_b32_e32 v19, v1
	v_cvt_pk_fp8_f32 v19, v10, v11
	v_pk_mul_f32 v[10:11], s[2:3], v[16:17] op_sel:[1,0]
	v_or_b32_e32 v0, 32, v36
	v_cvt_pk_fp8_f32 v18, v10, v11 op_sel:[0,0,1]
	v_mad_i64_i32 v[10:11], s[0:1], v0, s2, v[26:27]
	v_pk_mul_f32 v[6:7], s[2:3], v[6:7] op_sel:[1,0]
	v_pk_mul_f32 v[2:3], s[2:3], v[2:3] op_sel:[1,0]
	v_mov_b32_e32 v0, v1
	v_cvt_pk_fp8_f32 v0, v6, v7
	v_cvt_pk_fp8_f32 v1, v2, v3
	v_pk_mul_f32 v[12:13], s[2:3], v[12:13] op_sel:[1,0]
	v_pk_mul_f32 v[2:3], s[2:3], v[8:9] op_sel:[1,0]
	v_pk_mul_f32 v[4:5], s[2:3], v[4:5] op_sel:[1,0]
	v_cvt_pk_fp8_f32 v19, v12, v13 op_sel:[0,0,1]
	v_cvt_pk_fp8_f32 v0, v2, v3 op_sel:[0,0,1]
	v_cvt_pk_fp8_f32 v1, v4, v5 op_sel:[0,0,1]
	v_or_b32_e32 v2, 48, v36
	v_mad_i64_i32 v[2:3], s[0:1], v2, s2, v[26:27]
	global_store_dwordx2 v[10:11], v[18:19], off sc0 sc1
	global_store_dwordx2 v[2:3], v[0:1], off sc0 sc1
	s_endpgm
	.p2align	8

.LBB6_36:
	v_add_f32_e32 v64, v48, v49
	v_add_f32_e32 v64, v50, v64
	v_add_f32_e32 v64, v51, v64
	v_add_f32_e32 v64, v52, v64
	v_add_f32_e32 v68, v53, v64
	v_cvt_pk_f16_f32 v48, v48, v49
	v_cvt_pk_f16_f32 v49, v50, v51
	v_cvt_pk_f16_f32 v50, v52, v53
	v_cvt_pk_f16_f32 v51, v54, v55
	ds_read_b64_tr_b16 v[64:65], v207 offset:32768
	ds_read_b64_tr_b16 v[66:67], v207 offset:33280
	v_add_f32_e32 v52, v54, v68
	v_add_f32_e32 v68, v55, v52
	ds_read_b64_tr_b16 v[52:53], v207 offset:33792
	ds_read_b64_tr_b16 v[54:55], v207 offset:34304
	s_waitcnt lgkmcnt(2)
	v_mfma_f32_32x32x16_f16 v[0:15], v[48:51], v[64:67], v[0:15]
	ds_read_b64_tr_b16 v[64:65], v207 offset:36864
	ds_read_b64_tr_b16 v[66:67], v207 offset:37376
	v_add_f32_e32 v68, v56, v68
	v_add_f32_e32 v73, v57, v68
	v_cvt_pk_f16_f32 v68, v56, v57
	v_cvt_pk_f16_f32 v69, v58, v59
	v_cvt_pk_f16_f32 v70, v60, v61
	v_cvt_pk_f16_f32 v71, v62, v63
	s_waitcnt lgkmcnt(0)
	v_mfma_f32_32x32x16_f16 v[16:31], v[48:51], v[64:67], v[16:31]
	v_add_f32_e32 v48, v58, v73
	v_add_f32_e32 v48, v59, v48
	v_add_f32_e32 v48, v60, v48
	v_add_f32_e32 v48, v61, v48
	ds_read_b64_tr_b16 v[74:75], v207 offset:37888
	ds_read_b64_tr_b16 v[76:77], v207 offset:38400
	v_add_f32_e32 v48, v62, v48
	v_add_f32_e32 v48, v63, v48
	v_mfma_f32_32x32x16_f16 v[0:15], v[68:71], v[52:55], v[0:15]
	v_add_f32_e32 v48, v32, v48
	v_add_f32_e32 v56, v33, v48
	v_cvt_pk_f16_f32 v48, v32, v33
	v_cvt_pk_f16_f32 v49, v34, v35
	v_cvt_pk_f16_f32 v50, v36, v37
	v_cvt_pk_f16_f32 v51, v38, v39
	ds_read_b64_tr_b16 v[52:53], v207 offset:34816
	ds_read_b64_tr_b16 v[54:55], v207 offset:35328
	s_waitcnt lgkmcnt(2)
	v_mfma_f32_32x32x16_f16 v[16:31], v[68:71], v[74:77], v[16:31]
	v_add_f32_e32 v32, v34, v56
	v_add_f32_e32 v56, v35, v32
	ds_read_b64_tr_b16 v[32:33], v207 offset:35840
	ds_read_b64_tr_b16 v[34:35], v207 offset:36352
	v_add_f32_e32 v36, v36, v56
	v_add_f32_e32 v36, v37, v36
	v_cvt_pk_f16_f32 v56, v40, v41
	v_cvt_pk_f16_f32 v57, v42, v43
	s_waitcnt lgkmcnt(2)
	v_mfma_f32_32x32x16_f16 v[0:15], v[48:51], v[52:55], v[0:15]
	ds_read_b64_tr_b16 v[52:53], v207 offset:38912
	ds_read_b64_tr_b16 v[54:55], v207 offset:39424
	v_cvt_pk_f16_f32 v58, v44, v45
	v_cvt_pk_f16_f32 v59, v46, v47
	ds_read_b64_tr_b16 v[60:61], v207 offset:39936
	ds_read_b64_tr_b16 v[62:63], v207 offset:40448
	v_add_f32_e32 v36, v38, v36
	v_add_f32_e32 v36, v39, v36
	v_add_f32_e32 v36, v40, v36
	s_waitcnt lgkmcnt(2)
	v_mfma_f32_32x32x16_f16 v[16:31], v[48:51], v[52:55], v[16:31]
	v_add_f32_e32 v36, v41, v36
	v_mfma_f32_32x32x16_f16 v[0:15], v[56:59], v[32:35], v[0:15]
	v_add_f32_e32 v32, v42, v36
	v_add_f32_e32 v32, v43, v32
	v_add_f32_e32 v32, v44, v32
	v_add_f32_e32 v32, v45, v32
	v_add_f32_e32 v32, v46, v32
	v_add_f32_e32 v32, v47, v32
	v_add_f32_e32 v32, v72, v32
	s_waitcnt lgkmcnt(0)
	v_mfma_f32_32x32x16_f16 v[16:31], v[56:59], v[60:63], v[16:31]
	v_mov_b32_e32 v33, v32
	s_nop 1
	v_permlane32_swap_b32_e32 v32, v33
	s_and_saveexec_b64 s[2:3], s[0:1]
	v_add_f32_e32 v32, v32, v33
	ds_write_b32 v206, v32 offset:49280
	s_or_b64 exec, exec, s[2:3]
	s_waitcnt lgkmcnt(0)
	ds_read_b128 v[32:35], v205 offset:49280
	ds_read_b128 v[36:39], v205 offset:49312
	s_lshl_b64 s[0:1], s[18:19], 10
	s_add_u32 s0, s16, s0
	s_addc_u32 s1, s17, s1
	s_waitcnt lgkmcnt(1)
	v_rcp_f32_e32 v40, v32
	v_rcp_f32_e32 v41, v33
	v_rcp_f32_e32 v42, v34
	s_lshl_b32 s2, s33, 11
	v_mul_f32_e32 v40, 0x41800000, v40
	v_mul_f32_e32 v0, v0, v40
	v_mul_f32_e32 v16, v16, v40
	v_mov_b32_e32 v40, 0
	v_cvt_pk_fp8_f32 v40, v0, v16
	v_mul_f32_e32 v16, 0x41800000, v41
	v_mul_f32_e32 v1, v1, v16
	v_mul_f32_e32 v16, v17, v16
	v_mov_b32_e32 v17, 0
	v_cvt_pk_fp8_f32 v17, v1, v16
	s_add_i32 s2, s2, 0
	v_lshlrev_b32_e32 v0, 8, v204
	v_rcp_f32_e32 v43, v35
	v_add3_u32 v0, s2, v203, v0
	v_lshrrev_b32_e32 v1, 8, v40
	s_waitcnt lgkmcnt(0)
	v_rcp_f32_e32 v44, v36
	ds_read_b128 v[32:35], v205 offset:49344
	v_rcp_f32_e32 v45, v37
	v_rcp_f32_e32 v46, v38
	v_rcp_f32_e32 v47, v39
	ds_read_b128 v[36:39], v205 offset:49376
	s_waitcnt lgkmcnt(0)
	s_barrier
	ds_write_b8 v0, v40 offset:51200
	ds_write_b8 v0, v1 offset:51232
	ds_write_b8 v0, v17 offset:51264
	v_lshrrev_b32_e32 v1, 8, v17
	ds_write_b8 v0, v1 offset:51296
	v_mul_f32_e32 v1, 0x41800000, v42
	v_mul_f32_e32 v2, v2, v1
	v_mul_f32_e32 v1, v18, v1
	v_mov_b32_e32 v16, 0
	v_cvt_pk_fp8_f32 v16, v2, v1
	v_mul_f32_e32 v1, 0x41800000, v43
	v_mul_f32_e32 v2, v3, v1
	v_mul_f32_e32 v1, v19, v1
	v_mov_b32_e32 v3, 0
	v_cvt_pk_fp8_f32 v3, v2, v1
	v_lshrrev_b32_e32 v1, 8, v16
	ds_write_b8 v0, v16 offset:51328
	ds_write_b8 v0, v1 offset:51360
	ds_write_b8 v0, v3 offset:51392
	v_lshrrev_b32_e32 v1, 8, v3
	ds_write_b8 v0, v1 offset:51424
	v_mul_f32_e32 v1, 0x41800000, v44
	v_mul_f32_e32 v2, v4, v1
	v_mul_f32_e32 v1, v20, v1
	v_mov_b32_e32 v3, 0
	v_cvt_pk_fp8_f32 v3, v2, v1
	v_mul_f32_e32 v1, 0x41800000, v45
	v_mul_f32_e32 v2, v5, v1
	v_mul_f32_e32 v1, v21, v1
	v_mov_b32_e32 v4, 0
	v_cvt_pk_fp8_f32 v4, v2, v1
	v_lshrrev_b32_e32 v1, 8, v3
	ds_write_b8 v0, v3 offset:51712
	ds_write_b8 v0, v1 offset:51744
	ds_write_b8 v0, v4 offset:51776
	v_lshrrev_b32_e32 v1, 8, v4
	ds_write_b8 v0, v1 offset:51808
	v_mul_f32_e32 v1, 0x41800000, v46
	v_mul_f32_e32 v2, v6, v1
	v_mul_f32_e32 v1, v22, v1
	v_mov_b32_e32 v3, 0
	v_cvt_pk_fp8_f32 v3, v2, v1
	v_mul_f32_e32 v1, 0x41800000, v47
	v_mul_f32_e32 v2, v7, v1
	v_mul_f32_e32 v1, v23, v1
	v_mov_b32_e32 v4, 0
	v_cvt_pk_fp8_f32 v4, v2, v1
	s_waitcnt lgkmcnt(13)
	v_rcp_f32_e32 v32, v32
	v_rcp_f32_e32 v33, v33
	v_lshrrev_b32_e32 v1, 8, v3
	ds_write_b8 v0, v3 offset:51840
	ds_write_b8 v0, v1 offset:51872
	ds_write_b8 v0, v4 offset:51904
	v_lshrrev_b32_e32 v1, 8, v4
	ds_write_b8 v0, v1 offset:51936
	v_mul_f32_e32 v1, 0x41800000, v32
	v_mul_f32_e32 v2, v8, v1
	v_mul_f32_e32 v1, v24, v1
	v_mov_b32_e32 v3, 0
	v_cvt_pk_fp8_f32 v3, v2, v1
	v_mul_f32_e32 v1, 0x41800000, v33
	v_mul_f32_e32 v2, v9, v1
	v_mul_f32_e32 v1, v25, v1
	v_mov_b32_e32 v4, 0
	v_cvt_pk_fp8_f32 v4, v2, v1
	v_rcp_f32_e32 v34, v34
	v_rcp_f32_e32 v35, v35
	v_lshrrev_b32_e32 v1, 8, v3
	ds_write_b8 v0, v3 offset:52224
	ds_write_b8 v0, v1 offset:52256
	ds_write_b8 v0, v4 offset:52288
	v_lshrrev_b32_e32 v1, 8, v4
	ds_write_b8 v0, v1 offset:52320
	v_mul_f32_e32 v1, 0x41800000, v34
	v_mul_f32_e32 v2, v10, v1
	v_mul_f32_e32 v1, v26, v1
	v_mov_b32_e32 v3, 0
	v_cvt_pk_fp8_f32 v3, v2, v1
	v_mul_f32_e32 v1, 0x41800000, v35
	v_mul_f32_e32 v2, v11, v1
	v_mul_f32_e32 v1, v27, v1
	v_mov_b32_e32 v4, 0
	v_cvt_pk_fp8_f32 v4, v2, v1
	s_waitcnt lgkmcnt(14)
	v_rcp_f32_e32 v36, v36
	v_rcp_f32_e32 v37, v37
	v_lshrrev_b32_e32 v1, 8, v3
	ds_write_b8 v0, v3 offset:52352
	ds_write_b8 v0, v1 offset:52384
	ds_write_b8 v0, v4 offset:52416
	v_lshrrev_b32_e32 v1, 8, v4
	ds_write_b8 v0, v1 offset:52448
	v_mul_f32_e32 v1, 0x41800000, v36
	v_mul_f32_e32 v2, v12, v1
	v_mul_f32_e32 v1, v28, v1
	v_mov_b32_e32 v3, 0
	v_cvt_pk_fp8_f32 v3, v2, v1
	v_mul_f32_e32 v1, 0x41800000, v37
	v_mul_f32_e32 v2, v13, v1
	v_mul_f32_e32 v1, v29, v1
	v_mov_b32_e32 v4, 0
	v_cvt_pk_fp8_f32 v4, v2, v1
	v_rcp_f32_e32 v38, v38
	v_rcp_f32_e32 v39, v39
	v_lshrrev_b32_e32 v1, 8, v3
	ds_write_b8 v0, v3 offset:52736
	ds_write_b8 v0, v1 offset:52768
	ds_write_b8 v0, v4 offset:52800
	v_lshrrev_b32_e32 v1, 8, v4
	ds_write_b8 v0, v1 offset:52832
	v_mul_f32_e32 v1, 0x41800000, v38
	v_mul_f32_e32 v2, v14, v1
	v_mul_f32_e32 v1, v30, v1
	v_mov_b32_e32 v3, 0
	v_cvt_pk_fp8_f32 v3, v2, v1
	v_mul_f32_e32 v1, 0x41800000, v39
	v_mul_f32_e32 v2, v15, v1
	v_mul_f32_e32 v1, v31, v1
	v_mov_b32_e32 v4, 0
	v_cvt_pk_fp8_f32 v4, v2, v1
	v_lshrrev_b32_e32 v1, 8, v3
	ds_write_b8 v0, v3 offset:52864
	ds_write_b8 v0, v1 offset:52896
	ds_write_b8 v0, v4 offset:52928
	v_lshrrev_b32_e32 v1, 8, v4
	ds_write_b8 v0, v1 offset:52960
	v_add_u32_e32 v4, s2, v160
	s_waitcnt lgkmcnt(0)
	v_lshl_add_u32 v0, v202, 6, v4
	v_or_b32_e32 v12, 16, v202
	ds_read_b128 v[0:3], v0 offset:51200
	v_lshl_add_u32 v4, v12, 6, v4
	s_add_u32 s0, s0, s6
	ds_read_b128 v[4:7], v4 offset:51200
	v_mov_b32_e32 v161, 0
	s_addc_u32 s1, s1, 0
	v_lshl_add_u64 v[8:9], s[0:1], 0, v[160:161]
	v_lshlrev_b32_e32 v160, 10, v202
	v_lshl_add_u64 v[10:11], v[8:9], 0, v[160:161]
	v_lshlrev_b32_e32 v160, 10, v12
	s_waitcnt lgkmcnt(1)
	global_store_dwordx4 v[10:11], v[0:3], off sc0 sc1
	s_nop 1
	v_lshl_add_u64 v[0:1], v[8:9], 0, v[160:161]
	s_waitcnt lgkmcnt(0)
	global_store_dwordx4 v[0:1], v[4:7], off sc0 sc1
	s_waitcnt lgkmcnt(0)
	s_barrier
	s_endpgm

.LBB8_14:
	s_waitcnt vmcnt(0)
	v_cvt_f32_f16_sdwa v89, v68 dst_sel:DWORD dst_unused:UNUSED_PAD src0_sel:WORD_1
	v_cvt_f32_f16_e32 v88, v68
	v_cvt_f32_f16_sdwa v91, v69 dst_sel:DWORD dst_unused:UNUSED_PAD src0_sel:WORD_1
	v_cvt_f32_f16_e32 v90, v69
	s_waitcnt lgkmcnt(0)
	v_pk_add_f32 v[52:53], v[62:63], v[52:53]
	v_pk_add_f32 v[68:69], v[82:83], v[88:89]
	v_cvt_f32_f16_sdwa v83, v70 dst_sel:DWORD dst_unused:UNUSED_PAD src0_sel:WORD_1
	v_cvt_f32_f16_e32 v82, v70
	v_cvt_f32_f16_sdwa v89, v71 dst_sel:DWORD dst_unused:UNUSED_PAD src0_sel:WORD_1
	v_cvt_f32_f16_e32 v88, v71
	v_pk_add_f32 v[80:81], v[80:81], v[90:91]
	v_pk_add_f32 v[58:59], v[58:59], v[82:83]
	v_cvt_pk_f16_f32 v68, v68, v69
	v_cvt_pk_f16_f32 v70, v58, v59
	v_pk_add_f32 v[58:59], v[78:79], v[88:89]
	v_cvt_pk_f16_f32 v69, v80, v81
	v_cvt_pk_f16_f32 v71, v58, v59
	v_lshl_add_u64 v[58:59], v[76:77], 1, s[4:5]
	global_store_dwordx4 v[58:59], v[68:71], off sc0 sc1
	global_load_dwordx4 v[68:71], v[74:75], off offset:64
	v_cndmask_b32_e64 v62, 0, 1, s[8:9]
	v_pk_add_f32 v[56:57], v[66:67], v[56:57]
	v_pk_add_f32 v[54:55], v[64:65], v[54:55]
	v_cmp_ne_u32_e64 s[0:1], 1, v62
	s_andn2_b64 vcc, exec, s[8:9]
	v_pk_add_f32 v[50:51], v[60:61], v[50:51]
	s_cbranch_vccnz .LBB8_16
	global_load_dwordx4 v[60:63], v[72:73], off offset:128
	global_load_dwordx4 v[64:67], v[72:73], off offset:144
	s_waitcnt vmcnt(1)
	v_pk_add_f32 v[56:57], v[56:57], v[62:63]
	v_pk_add_f32 v[54:55], v[54:55], v[60:61]
	s_waitcnt vmcnt(0)
	v_pk_add_f32 v[52:53], v[52:53], v[66:67]
	v_pk_add_f32 v[50:51], v[50:51], v[64:65]
.LBB8_16:
	s_waitcnt vmcnt(0)
	v_cvt_f32_f16_sdwa v61, v68 dst_sel:DWORD dst_unused:UNUSED_PAD src0_sel:WORD_1
	v_cvt_f32_f16_e32 v60, v68
	v_cvt_f32_f16_sdwa v63, v69 dst_sel:DWORD dst_unused:UNUSED_PAD src0_sel:WORD_1
	v_cvt_f32_f16_e32 v62, v69
	v_or_b32_e32 v74, 48, v85
	v_pk_add_f32 v[54:55], v[54:55], v[60:61]
	v_cvt_f32_f16_sdwa v61, v70 dst_sel:DWORD dst_unused:UNUSED_PAD src0_sel:WORD_1
	v_cvt_f32_f16_e32 v60, v70
	v_pk_add_f32 v[56:57], v[56:57], v[62:63]
	v_cvt_f32_f16_sdwa v63, v71 dst_sel:DWORD dst_unused:UNUSED_PAD src0_sel:WORD_1
	v_cvt_f32_f16_e32 v62, v71
	v_pk_add_f32 v[50:51], v[50:51], v[60:61]
	v_cvt_pk_f16_f32 v54, v54, v55
	v_cvt_pk_f16_f32 v55, v56, v57
	v_cvt_pk_f16_f32 v56, v50, v51
	v_pk_add_f32 v[50:51], v[52:53], v[62:63]
	v_mad_i64_i32 v[60:61], s[8:9], v74, s10, v[0:1]
	v_cvt_pk_f16_f32 v57, v50, v51
	global_store_dwordx4 v[58:59], v[54:57], off offset:64 sc0 sc1
	v_lshl_add_u64 v[58:59], v[60:61], 1, s[2:3]
	global_load_dwordx4 v[50:53], v[58:59], off
	ds_read_b128 v[54:57], v86 offset:4096
	ds_read_b128 v[68:71], v86 offset:5120
	s_and_b64 vcc, exec, s[0:1]
	s_waitcnt lgkmcnt(1)
	v_pk_add_f32 v[64:65], v[56:57], v[48:49]
	v_pk_add_f32 v[66:67], v[54:55], v[46:47]
	s_waitcnt lgkmcnt(0)
	v_pk_add_f32 v[62:63], v[70:71], v[44:45]
	ds_read_b128 v[54:57], v86 offset:6144
	ds_read_b128 v[44:47], v86 offset:7168
	v_pk_add_f32 v[42:43], v[68:69], v[42:43]
	v_mad_i64_i32 v[48:49], s[8:9], v74, s10, 0
	s_cbranch_vccnz .LBB8_18
	global_load_dwordx4 v[68:71], v[72:73], off
	global_load_dwordx4 v[74:77], v[72:73], off offset:16
	s_waitcnt vmcnt(1)
	v_pk_add_f32 v[64:65], v[64:65], v[70:71]
	v_pk_add_f32 v[66:67], v[66:67], v[68:69]
	s_waitcnt vmcnt(0)
	v_pk_add_f32 v[62:63], v[62:63], v[76:77]
	v_pk_add_f32 v[42:43], v[42:43], v[74:75]
.LBB8_18:
	s_waitcnt lgkmcnt(0)
	v_pk_add_f32 v[34:35], v[44:45], v[34:35]
	s_waitcnt vmcnt(0)
	v_cvt_f32_f16_sdwa v45, v50 dst_sel:DWORD dst_unused:UNUSED_PAD src0_sel:WORD_1
	v_cvt_f32_f16_e32 v44, v50
	v_pk_add_f32 v[38:39], v[54:55], v[38:39]
	v_cvt_f32_f16_sdwa v55, v51 dst_sel:DWORD dst_unused:UNUSED_PAD src0_sel:WORD_1
	v_cvt_f32_f16_e32 v54, v51
	v_pk_add_f32 v[44:45], v[66:67], v[44:45]
	v_pk_add_f32 v[40:41], v[56:57], v[40:41]
	v_cvt_pk_f16_f32 v50, v44, v45
	v_pk_add_f32 v[44:45], v[64:65], v[54:55]
	v_cvt_f32_f16_sdwa v55, v52 dst_sel:DWORD dst_unused:UNUSED_PAD src0_sel:WORD_1
	v_cvt_f32_f16_e32 v54, v52
	v_cvt_f32_f16_sdwa v57, v53 dst_sel:DWORD dst_unused:UNUSED_PAD src0_sel:WORD_1
	v_cvt_f32_f16_e32 v56, v53
	v_pk_add_f32 v[36:37], v[46:47], v[36:37]
	v_pk_add_f32 v[42:43], v[42:43], v[54:55]
	v_or_b32_e32 v46, 32, v0
	v_cvt_pk_f16_f32 v52, v42, v43
	v_pk_add_f32 v[42:43], v[62:63], v[56:57]
	v_mov_b32_e32 v47, 0
	v_cvt_pk_f16_f32 v51, v44, v45
	v_cvt_pk_f16_f32 v53, v42, v43
	v_lshl_add_u64 v[42:43], v[60:61], 1, s[4:5]
	s_and_b64 vcc, exec, s[0:1]
	global_store_dwordx4 v[42:43], v[50:53], off sc0 sc1
	s_cbranch_vccnz .LBB8_20
	global_load_dwordx4 v[42:45], v[72:73], off offset:128
	global_load_dwordx4 v[50:53], v[72:73], off offset:144
	s_waitcnt vmcnt(1)
	v_pk_add_f32 v[40:41], v[40:41], v[44:45]
	v_pk_add_f32 v[38:39], v[38:39], v[42:43]
	s_waitcnt vmcnt(0)
	v_pk_add_f32 v[36:37], v[36:37], v[52:53]
	v_pk_add_f32 v[34:35], v[34:35], v[50:51]

.LBB8_24:
	s_waitcnt vmcnt(0)
	v_cvt_f32_f16_sdwa v31, v42 dst_sel:DWORD dst_unused:UNUSED_PAD src0_sel:WORD_1
	v_cvt_f32_f16_e32 v30, v42
	v_cvt_f32_f16_sdwa v33, v43 dst_sel:DWORD dst_unused:UNUSED_PAD src0_sel:WORD_1
	v_cvt_f32_f16_e32 v32, v43
	s_waitcnt lgkmcnt(1)
	v_pk_add_f32 v[24:25], v[40:41], v[24:25]
	v_pk_add_f32 v[30:31], v[54:55], v[30:31]
	v_pk_add_f32 v[22:23], v[38:39], v[22:23]
	v_cvt_pk_f16_f32 v42, v30, v31
	v_pk_add_f32 v[30:31], v[52:53], v[32:33]
	v_cvt_f32_f16_sdwa v33, v44 dst_sel:DWORD dst_unused:UNUSED_PAD src0_sel:WORD_1
	v_cvt_f32_f16_e32 v32, v44
	v_cvt_f32_f16_sdwa v53, v45 dst_sel:DWORD dst_unused:UNUSED_PAD src0_sel:WORD_1
	v_cvt_f32_f16_e32 v52, v45
	v_cvt_pk_f16_f32 v43, v30, v31
	v_pk_add_f32 v[28:29], v[28:29], v[32:33]
	v_lshl_add_u64 v[30:31], v[50:51], 1, s[4:5]
	v_pk_add_f32 v[26:27], v[26:27], v[52:53]
	v_cvt_pk_f16_f32 v44, v28, v29
	v_cvt_pk_f16_f32 v45, v26, v27
	global_store_dwordx4 v[30:31], v[42:45], off sc0 sc1
	global_load_dwordx4 v[26:29], v[48:49], off offset:64
	v_cndmask_b32_e64 v32, 0, 1, s[8:9]
	s_waitcnt lgkmcnt(0)
	v_pk_add_f32 v[20:21], v[36:37], v[20:21]
	v_cmp_ne_u32_e64 s[0:1], 1, v32
	s_andn2_b64 vcc, exec, s[8:9]
	v_pk_add_f32 v[18:19], v[34:35], v[18:19]
	s_cbranch_vccnz .LBB8_26
	global_load_dwordx4 v[32:35], v[46:47], off offset:128
	global_load_dwordx4 v[36:39], v[46:47], off offset:144
	s_waitcnt vmcnt(1)
	v_pk_add_f32 v[24:25], v[24:25], v[34:35]
	v_pk_add_f32 v[22:23], v[22:23], v[32:33]
	s_waitcnt vmcnt(0)
	v_pk_add_f32 v[20:21], v[20:21], v[38:39]
	v_pk_add_f32 v[18:19], v[18:19], v[36:37]
.LBB8_26:
	s_waitcnt vmcnt(0)
	v_cvt_f32_f16_sdwa v33, v26 dst_sel:DWORD dst_unused:UNUSED_PAD src0_sel:WORD_1
	v_cvt_f32_f16_e32 v32, v26
	v_cvt_f32_f16_sdwa v35, v27 dst_sel:DWORD dst_unused:UNUSED_PAD src0_sel:WORD_1
	v_cvt_f32_f16_e32 v34, v27
	v_cvt_f32_f16_sdwa v27, v28 dst_sel:DWORD dst_unused:UNUSED_PAD src0_sel:WORD_1
	v_cvt_f32_f16_e32 v26, v28
	v_pk_add_f32 v[22:23], v[22:23], v[32:33]
	v_cvt_f32_f16_sdwa v33, v29 dst_sel:DWORD dst_unused:UNUSED_PAD src0_sel:WORD_1
	v_cvt_f32_f16_e32 v32, v29
	v_pk_add_f32 v[24:25], v[24:25], v[34:35]
	v_pk_add_f32 v[18:19], v[18:19], v[26:27]
	v_cvt_pk_f16_f32 v22, v22, v23
	v_cvt_pk_f16_f32 v23, v24, v25
	v_cvt_pk_f16_f32 v24, v18, v19
	v_pk_add_f32 v[18:19], v[20:21], v[32:33]
	v_or_b32_e32 v38, 16, v85
	v_cvt_pk_f16_f32 v25, v18, v19
	v_mad_i64_i32 v[28:29], s[6:7], v38, s10, v[0:1]
	global_store_dwordx4 v[30:31], v[22:25], off offset:64 sc0 sc1
	v_lshl_add_u64 v[26:27], v[28:29], 1, s[2:3]
	global_load_dwordx4 v[18:21], v[26:27], off
	ds_read_b128 v[22:25], v56 offset:36864
	ds_read_b128 v[34:37], v56 offset:37888
	s_and_b64 vcc, exec, s[0:1]
	s_waitcnt lgkmcnt(1)
	v_pk_add_f32 v[32:33], v[24:25], v[16:17]
	v_pk_add_f32 v[42:43], v[22:23], v[14:15]
	s_waitcnt lgkmcnt(0)
	v_pk_add_f32 v[16:17], v[36:37], v[12:13]
	ds_read_b128 v[22:25], v56 offset:38912
	ds_read_b128 v[12:15], v56 offset:39936
	v_pk_add_f32 v[30:31], v[34:35], v[10:11]
	v_mad_i64_i32 v[10:11], s[2:3], v38, s10, 0
	s_cbranch_vccnz .LBB8_28
	global_load_dwordx4 v[34:37], v[46:47], off
	global_load_dwordx4 v[38:41], v[46:47], off offset:16
	s_waitcnt vmcnt(1)
	v_pk_add_f32 v[32:33], v[32:33], v[36:37]
	v_pk_add_f32 v[42:43], v[42:43], v[34:35]
	s_waitcnt vmcnt(0)
	v_pk_add_f32 v[16:17], v[16:17], v[40:41]
	v_pk_add_f32 v[30:31], v[30:31], v[38:39]
.LBB8_28:
	s_waitcnt lgkmcnt(0)
	v_pk_add_f32 v[36:37], v[14:15], v[4:5]
	v_pk_add_f32 v[34:35], v[12:13], v[2:3]
	s_waitcnt vmcnt(0)
	v_cvt_f32_f16_sdwa v3, v18 dst_sel:DWORD dst_unused:UNUSED_PAD src0_sel:WORD_1
	v_cvt_f32_f16_e32 v2, v18
	v_cvt_f32_f16_sdwa v5, v19 dst_sel:DWORD dst_unused:UNUSED_PAD src0_sel:WORD_1
	v_cvt_f32_f16_e32 v4, v19
	v_pk_add_f32 v[40:41], v[24:25], v[8:9]
	v_pk_add_f32 v[38:39], v[22:23], v[6:7]
	v_cvt_f32_f16_sdwa v7, v20 dst_sel:DWORD dst_unused:UNUSED_PAD src0_sel:WORD_1
	v_cvt_f32_f16_e32 v6, v20
	v_cvt_f32_f16_sdwa v9, v21 dst_sel:DWORD dst_unused:UNUSED_PAD src0_sel:WORD_1
	v_cvt_f32_f16_e32 v8, v21
	v_pk_add_f32 v[2:3], v[42:43], v[2:3]
	v_pk_add_f32 v[4:5], v[32:33], v[4:5]
	v_cvt_pk_f16_f32 v2, v2, v3
	v_cvt_pk_f16_f32 v3, v4, v5
	v_pk_add_f32 v[4:5], v[30:31], v[6:7]
	v_pk_add_f32 v[6:7], v[16:17], v[8:9]
	v_or_b32_e32 v0, 32, v0
	v_mov_b32_e32 v1, 0
	v_cvt_pk_f16_f32 v4, v4, v5
	v_cvt_pk_f16_f32 v5, v6, v7
	v_lshl_add_u64 v[6:7], v[28:29], 1, s[4:5]
	s_and_b64 vcc, exec, s[0:1]
	global_store_dwordx4 v[6:7], v[2:5], off sc0 sc1
	s_cbranch_vccnz .LBB8_30
	global_load_dwordx4 v[2:5], v[46:47], off offset:128
	global_load_dwordx4 v[6:9], v[46:47], off offset:144
	s_waitcnt vmcnt(1)
	v_pk_add_f32 v[40:41], v[40:41], v[4:5]
	v_pk_add_f32 v[38:39], v[38:39], v[2:3]
	s_waitcnt vmcnt(0)
	v_pk_add_f32 v[36:37], v[36:37], v[8:9]
	v_pk_add_f32 v[34:35], v[34:35], v[6:7]

.LBB8_31:
	s_waitcnt vmcnt(0)
	v_cvt_f32_f16_sdwa v1, v42 dst_sel:DWORD dst_unused:UNUSED_PAD src0_sel:WORD_1
	v_cvt_f32_f16_e32 v0, v42
	v_cvt_f32_f16_sdwa v3, v43 dst_sel:DWORD dst_unused:UNUSED_PAD src0_sel:WORD_1
	v_cvt_f32_f16_e32 v2, v43
	v_cvt_f32_f16_sdwa v5, v44 dst_sel:DWORD dst_unused:UNUSED_PAD src0_sel:WORD_1
	v_cvt_f32_f16_e32 v4, v44
	v_cvt_f32_f16_sdwa v7, v45 dst_sel:DWORD dst_unused:UNUSED_PAD src0_sel:WORD_1
	v_cvt_f32_f16_e32 v6, v45
	v_pk_add_f32 v[0:1], v[38:39], v[0:1]
	v_pk_add_f32 v[2:3], v[40:41], v[2:3]
	v_cvt_pk_f16_f32 v0, v0, v1
	v_cvt_pk_f16_f32 v1, v2, v3
	v_pk_add_f32 v[2:3], v[34:35], v[4:5]
	v_pk_add_f32 v[4:5], v[36:37], v[6:7]
	v_cvt_pk_f16_f32 v2, v2, v3
	v_cvt_pk_f16_f32 v3, v4, v5
	v_lshl_add_u64 v[4:5], v[46:47], 1, s[4:5]
	global_store_dwordx4 v[4:5], v[0:3], off sc0 sc1
	s_endpgm
	.p2align	8
